# baseline (speedup 1.0000x reference)
_Z12route_kernelPKyPiP15HIP_vector_typeIiLj4EES1_:
	s_load_dwordx2 s[6:7], s[0:1], 0x0
	s_load_dwordx2 s[4:5], s[0:1], 0x10
	s_load_dwordx2 s[14:15], s[0:1], 0x8
	s_load_dwordx2 s[16:17], s[0:1], 0x18
	s_movk_i32 s2, 0x100
	v_cmp_gt_u32_e32 vcc, s2, v0
	s_and_saveexec_b64 s[2:3], vcc
	v_lshlrev_b32_e32 v1, 2, v0
	v_mov_b32_e32 v2, 0
	ds_write2st64_b32 v1, v2, v2 offset1:4
	s_or_b64 exec, exec, s[2:3]
	s_movk_i32 s2, 0x148
	v_cmp_gt_u32_e64 s[2:3], s2, v0
	v_mov_b32_e32 v9, 0
	s_and_saveexec_b64 s[8:9], s[2:3]
	s_cbranch_execz .LBB2_4
	v_mov_b32_e32 v2, 0
	v_lshlrev_b32_e32 v1, 4, v0
	v_mov_b32_e32 v3, v2
	v_mov_b32_e32 v4, v2
	v_mov_b32_e32 v5, v2
	s_waitcnt lgkmcnt(0)
	global_store_dwordx4 v1, v[2:5], s[4:5]

.LBB2_8:
	s_or_b64 exec, exec, s[6:7]
	s_mov_b64 s[2:3], s[14:15]
	s_waitcnt lgkmcnt(0)
	s_barrier
	s_and_saveexec_b64 s[6:7], vcc
	s_cbranch_execz .LBB2_15
	s_mov_b64 s[0:1], s[16:17]
	v_cmp_lt_u32_e32 vcc, 63, v0
	s_and_saveexec_b64 s[8:9], vcc
	s_cbranch_execz .LBB2_13
	s_movk_i32 s12, 0x1000
	s_mov_b64 s[10:11], 0

	.amdhsa_kernel _Z12route_kernelPKyPiP15HIP_vector_typeIiLj4EES1_
		.amdhsa_group_segment_fixed_size 4128
		.amdhsa_private_segment_fixed_size 0
		.amdhsa_kernarg_size 32
		.amdhsa_user_sgpr_count 2
		.amdhsa_user_sgpr_dispatch_ptr 0
		.amdhsa_user_sgpr_queue_ptr 0
		.amdhsa_user_sgpr_kernarg_segment_ptr 1
		.amdhsa_user_sgpr_dispatch_id 0
		.amdhsa_user_sgpr_kernarg_preload_length 0
		.amdhsa_user_sgpr_kernarg_preload_offset 0
		.amdhsa_user_sgpr_private_segment_size 0
		.amdhsa_uses_dynamic_stack 0
		.amdhsa_enable_private_segment 0
		.amdhsa_system_sgpr_workgroup_id_x 1
		.amdhsa_system_sgpr_workgroup_id_y 0
		.amdhsa_system_sgpr_workgroup_id_z 0
		.amdhsa_system_sgpr_workgroup_info 0
		.amdhsa_system_vgpr_workitem_id 0
		.amdhsa_next_free_vgpr 23
		.amdhsa_next_free_sgpr 18
		.amdhsa_accum_offset 24
		.amdhsa_reserve_vcc 1
		.amdhsa_float_round_mode_32 0
		.amdhsa_float_round_mode_16_64 0
		.amdhsa_float_denorm_mode_32 3
		.amdhsa_float_denorm_mode_16_64 3
		.amdhsa_dx10_clamp 1
		.amdhsa_ieee_mode 1
		.amdhsa_fp16_overflow 0
		.amdhsa_tg_split 0
		.amdhsa_exception_fp_ieee_invalid_op 0
		.amdhsa_exception_fp_denorm_src 0
		.amdhsa_exception_fp_ieee_div_zero 0
		.amdhsa_exception_fp_ieee_overflow 0
		.amdhsa_exception_fp_ieee_underflow 0
		.amdhsa_exception_fp_ieee_inexact 0
		.amdhsa_exception_int_div_zero 0
	.end_amdhsa_kernel
